# baseline (speedup 1.0000x reference)
.LBB1_237:
	s_ashr_i32 s5, s4, 31
	s_and_b32 s30, s20, 0x3ff
	s_lshl_b64 s[0:1], s[4:5], 24
	s_add_u32 s0, s16, s0
	s_addc_u32 s1, s17, s1
	v_add_u32_e32 v79, s30, v149
	v_mov_b32_e32 v78, v61
	s_cmpk_lt_u32 s20, 0x400
	s_waitcnt vmcnt(0)
	v_pk_mul_f32 v[80:81], v[78:79], v[68:69] op_sel:[0,1] op_sel_hi:[0,0]
	v_mov_b32_e32 v72, s28
	s_cselect_b64 vcc, -1, 0
	v_pk_fma_f32 v[82:83], v[60:61], v[68:69], v[80:81] neg_lo:[0,0,1] neg_hi:[0,0,1]
	v_pk_fma_f32 v[60:61], v[60:61], v[68:69], v[80:81] op_sel_hi:[0,1,1]
	v_mov_b32_e32 v78, v63
	v_cndmask_b32_e32 v72, 1.0, v72, vcc
	v_mov_b32_e32 v83, v61
	v_pk_mul_f32 v[80:81], v[78:79], v[70:71] op_sel:[0,1] op_sel_hi:[0,0]
	v_pk_mul_f32 v[60:61], v[72:73], v[82:83] op_sel_hi:[0,1]
	v_pk_fma_f32 v[82:83], v[62:63], v[70:71], v[80:81] neg_lo:[0,0,1] neg_hi:[0,0,1]
	v_pk_fma_f32 v[62:63], v[62:63], v[70:71], v[80:81] op_sel_hi:[0,1,1]
	v_mov_b32_e32 v78, v57
	v_mov_b32_e32 v83, v63
	v_pk_mul_f32 v[80:81], v[78:79], v[64:65] op_sel:[0,1] op_sel_hi:[0,0]
	v_pk_mul_f32 v[62:63], v[72:73], v[82:83] op_sel_hi:[0,1]
	v_pk_fma_f32 v[82:83], v[56:57], v[64:65], v[80:81] neg_lo:[0,0,1] neg_hi:[0,0,1]
	v_pk_fma_f32 v[56:57], v[56:57], v[64:65], v[80:81] op_sel_hi:[0,1,1]
	v_mov_b32_e32 v56, v59
	v_mov_b32_e32 v83, v57
	v_pk_mul_f32 v[56:57], v[56:57], v[66:67] op_sel:[0,1] op_sel_hi:[0,0]
	v_pk_mul_f32 v[80:81], v[72:73], v[82:83] op_sel_hi:[0,1]
	v_pk_fma_f32 v[82:83], v[58:59], v[66:67], v[56:57] neg_lo:[0,0,1] neg_hi:[0,0,1]
	v_pk_fma_f32 v[56:57], v[58:59], v[66:67], v[56:57] op_sel_hi:[0,1,1]
	v_lshlrev_b32_e32 v136, 1, v79
	s_cmp_lg_u32 s4, 2
	v_ashrrev_i32_e32 v77, 31, v76
	v_mov_b32_e32 v83, v57
	v_lshl_add_u64 v[74:75], s[0:1], 0, v[136:137]
	s_cselect_b64 s[4:5], -1, 0
	v_lshlrev_b64 v[76:77], 11, v[76:77]
	v_pk_mul_f32 v[82:83], v[72:73], v[82:83] op_sel_hi:[0,1]
	v_lshl_add_u64 v[76:77], v[74:75], 0, v[76:77]
	v_cvt_pk_f16_f32 v56, v60, v61
	v_cvt_pk_f16_f32 v57, v62, v63
	v_cvt_pk_f16_f32 v58, v80, v81
	v_cvt_pk_f16_f32 v59, v82, v83
	s_mov_b64 s[30:31], -1
	s_and_b64 vcc, exec, s[4:5]
	s_cbranch_vccz .LBB1_239
	global_store_dwordx4 v[76:77], v[56:59], off sc1
	s_mov_b64 s[30:31], 0
.LBB1_239:
	v_lshlrev_b32_e32 v60, 7, v79
	v_and_b32_e32 v136, 0x1000, v60
	v_and_b32_e32 v62, 24, v79
	s_ashr_i32 s20, s35, 7
	v_lshl_add_u64 v[60:61], s[0:1], 0, v[136:137]
	v_lshlrev_b32_e32 v136, 1, v62
	s_and_b32 s20, s20, -16
	v_lshl_add_u64 v[60:61], v[60:61], 0, v[136:137]
	v_mov_b32_e32 v141, v137
	v_lshrrev_b32_e32 v73, 6, v79
	s_bfe_u32 s34, s35, 0x50006
	v_lshl_add_u64 v[62:63], v[60:61], 0, v[140:141]
	s_andn2_b64 vcc, exec, s[30:31]
	v_add_u32_e32 v78, s20, v73
	s_cbranch_vccnz .LBB1_241
	v_lshl_or_b32 v80, v78, 5, s34
	v_ashrrev_i32_e32 v81, 31, v80
	v_lshlrev_b64 v[80:81], 13, v[80:81]
	v_lshl_add_u64 v[80:81], v[62:63], 0, v[80:81]
	global_store_dwordx4 v[80:81], v[56:59], off sc1
.LBB1_241:
	v_mov_b64_e32 v[86:87], v[80:81]
	s_mov_b32 s0, 0x80000
	s_mov_b32 s1, 0
	v_lshl_add_u64 v[88:89], v[80:81], 0, s[0:1]
	v_cvt_pk_f16_f32 v64, v52, v53
	v_cvt_pk_f16_f32 v65, v54, v55
	v_cvt_pk_f16_f32 v66, v48, v49
	v_cvt_pk_f16_f32 v67, v50, v51
	global_store_dwordx4 v[88:89], v[64:67], off sc1
	v_cvt_pk_f16_f32 v68, v44, v45
	v_cvt_pk_f16_f32 v69, v46, v47
	v_cvt_pk_f16_f32 v70, v40, v41
	v_cvt_pk_f16_f32 v71, v42, v43
	global_store_dwordx4 v[86:87], v[68:71], off offset:1024 sc1
	v_cvt_pk_f16_f32 v72, v36, v37
	v_cvt_pk_f16_f32 v73, v38, v39
	v_cvt_pk_f16_f32 v74, v32, v33
	v_cvt_pk_f16_f32 v75, v34, v35
	global_store_dwordx4 v[88:89], v[72:75], off offset:1024 sc1
	v_cvt_pk_f16_f32 v76, v28, v29
	v_cvt_pk_f16_f32 v77, v30, v31
	v_cvt_pk_f16_f32 v78, v24, v25
	v_cvt_pk_f16_f32 v79, v26, v27
	global_store_dwordx4 v[86:87], v[76:79], off offset:2048 sc1
	v_cvt_pk_f16_f32 v64, v20, v21
	v_cvt_pk_f16_f32 v65, v22, v23
	v_cvt_pk_f16_f32 v66, v16, v17
	v_cvt_pk_f16_f32 v67, v18, v19
	global_store_dwordx4 v[88:89], v[64:67], off offset:2048 sc1
	v_cvt_pk_f16_f32 v68, v12, v13
	v_cvt_pk_f16_f32 v69, v14, v15
	v_cvt_pk_f16_f32 v70, v8, v9
	v_cvt_pk_f16_f32 v71, v10, v11
	global_store_dwordx4 v[86:87], v[68:71], off offset:3072 sc1
	v_cvt_pk_f16_f32 v72, v4, v5
	v_cvt_pk_f16_f32 v73, v6, v7
	v_cvt_pk_f16_f32 v74, v0, v1
	v_cvt_pk_f16_f32 v75, v2, v3
	global_store_dwordx4 v[88:89], v[72:75], off offset:3072 sc1
	s_branch .LBB1_217
